# speedup vs baseline: 1.0062x; 1.0062x over previous
.LBB11_26:
	s_and_b64 vcc, exec, s[4:5]
	s_cbranch_vccz .LBB11_38
	s_waitcnt lgkmcnt(0)
	s_load_dwordx4 s[4:7], s[0:1], 0x0
	s_waitcnt lgkmcnt(0)
	s_sub_u32 s4, s6, s4
	s_cmp_lg_u32 s4, 0x62d2700
	s_cbranch_scc1 .LBB11_38
	s_waitcnt lgkmcnt(0)
	s_load_dword s10, s[0:1], 0x60
	s_lshl_b32 s4, s2, 9
	v_or_b32_e32 v1, s4, v0
	v_add_u32_e32 v2, 0xfffe8000, v1
	s_waitcnt lgkmcnt(0)
	v_cmp_gt_i32_e32 vcc, s10, v2
	s_and_saveexec_b64 s[2:3], vcc
	s_cbranch_execz .LBB11_38
	v_add_u32_e32 v0, s4, v0
	v_add_u32_e32 v1, 0xffff0000, v0
	s_load_dwordx2 s[2:3], s[0:1], 0x58
	v_max_i32_e32 v1, s10, v1
	v_sub_u32_e32 v0, v1, v0
	v_add_u32_e32 v5, 0x17fff, v0
	s_mov_b32 s0, 0x38000
	v_and_b32_e32 v0, 0x38000, v5
	v_cmp_ne_u32_e32 vcc, s0, v0
	v_mov_b32_e32 v4, 0
	s_and_saveexec_b64 s[0:1], vcc
	s_cbranch_execz .LBB11_32
	v_lshrrev_b32_e32 v0, 15, v5
	v_add_u32_e32 v0, 1, v0
	v_ashrrev_i32_e32 v3, 31, v2
	v_and_b32_e32 v4, 7, v0
	s_waitcnt lgkmcnt(0)
	v_lshl_add_u64 v[0:1], v[2:3], 4, s[2:3]
	v_lshl_add_u64 v[0:1], v[0:1], 0, 12
	v_sub_u32_e32 v3, 0, v4
	v_mov_b32_e32 v4, 0
	s_mov_b64 s[4:5], 0
	s_mov_b64 s[6:7], 0x80000

.LBB11_38:
	s_endpgm
	s_nop 0
	s_endpgm

.LBB12_2:
	s_andn2_b64 vcc, exec, s[4:5]
	s_cbranch_vccnz .LBB12_14
	s_waitcnt lgkmcnt(0)
	s_load_dwordx4 s[4:7], s[0:1], 0x0
	s_waitcnt lgkmcnt(0)
	s_sub_u32 s4, s6, s4
	s_cmp_lg_u32 s4, 0x4dfa700
	s_cbranch_scc1 .LBB12_14
	s_load_dword s10, s[0:1], 0x60
	s_lshl_b32 s6, s2, 9
	v_or_b32_e32 v1, s6, v0
	v_add_u32_e32 v2, 0xfffe8000, v1
	s_waitcnt lgkmcnt(0)
	v_cmp_gt_i32_e32 vcc, s10, v2
	s_and_saveexec_b64 s[2:3], vcc
	s_cbranch_execz .LBB12_14
	v_add_u32_e32 v0, s6, v0
	v_add_u32_e32 v1, 0xffff0000, v0
	s_load_dwordx2 s[4:5], s[0:1], 0x58
	s_load_dwordx2 s[2:3], s[0:1], 0x68
	v_max_i32_e32 v1, s10, v1
	v_sub_u32_e32 v0, v1, v0
	v_add_u32_e32 v5, 0x17fff, v0
	s_mov_b32 s0, 0x38000
	v_and_b32_e32 v0, 0x38000, v5
	v_cmp_ne_u32_e32 vcc, s0, v0
	v_mov_b32_e32 v4, 0
	s_and_saveexec_b64 s[0:1], vcc
	s_cbranch_execz .LBB12_8
	v_lshrrev_b32_e32 v0, 15, v5
	v_add_u32_e32 v0, 1, v0
	v_ashrrev_i32_e32 v3, 31, v2
	v_and_b32_e32 v4, 7, v0
	s_waitcnt lgkmcnt(0)
	v_lshl_add_u64 v[0:1], v[2:3], 4, s[4:5]
	v_lshl_add_u64 v[0:1], v[0:1], 0, 12
	v_sub_u32_e32 v3, 0, v4
	v_mov_b32_e32 v4, 0
	s_mov_b64 s[6:7], 0
	s_mov_b64 s[8:9], 0x80000

.LBB12_14:
	s_endpgm
	s_nop 0
	s_nop 0
	s_nop 0
	s_nop 0
	s_nop 0
	s_nop 0
	s_nop 0
	s_nop 0
	s_nop 0
	s_nop 0
	s_nop 0
	s_nop 0
	s_nop 0
	s_nop 0
	s_nop 0
	s_nop 0
	s_nop 0
	s_nop 0
	s_nop 0
	s_nop 0
	s_nop 0
	s_nop 0
	s_nop 0
	s_nop 0
	s_nop 0
	s_nop 0
	s_nop 0
	s_nop 0
	s_nop 0
	s_nop 0
	s_nop 0
	s_nop 0
	s_nop 0
	s_nop 0
	s_nop 0
	s_nop 0
	s_nop 0
	s_nop 0
	s_nop 0
	s_nop 0
	s_nop 0
	s_nop 0
	s_nop 0
	s_nop 0
	s_nop 0
	s_nop 0
	s_nop 0
	s_nop 0
	s_nop 0
	s_nop 0
	s_nop 0
	s_nop 0
	s_nop 0
	s_nop 0
	s_nop 0
	s_nop 0
	s_nop 0
	s_nop 0
	s_nop 0
	s_nop 0
	s_endpgm
